# out-projection epilogue: nt hint on the read-once f32 residual input rows
# baseline (speedup 1.0000x reference)
.LBB0_752:
	s_lshl_b32 s8, s34, 8
	s_lshr_b32 s34, s33, 5
	s_mulk_i32 s34, 0x1800
	s_ashr_i32 s35, s34, 31
	s_or_b32 s8, s8, s63
	s_lshl_b32 s46, s33, 8
	s_lshl_b64 s[34:35], s[34:35], 2
	v_or_b32_e32 v114, s8, v182
	s_add_u32 s34, s72, s34
	s_addc_u32 s35, s73, s35
	v_ashrrev_i32_e32 v115, 31, v114
	v_lshl_add_u64 v[114:115], v[114:115], 2, s[34:35]
	v_lshl_add_u64 v[116:117], v[114:115], 0, s[20:21]
	v_add_co_u32_e32 v114, vcc, s80, v114
	global_load_dwordx4 v[130:133], v[116:117], off offset:16
	global_load_dwordx4 v[118:121], v[116:117], off offset:512
	v_addc_co_u32_e32 v115, vcc, 0, v115, vcc
	global_load_dwordx4 v[134:137], v[114:115], off
	s_nop 0
	global_load_dwordx4 v[114:117], v[116:117], off offset:528
	v_add_u32_e32 v176, s46, v152
	v_or_b32_e32 v172, s8, v184
	v_ashrrev_i32_e32 v177, 31, v176
	v_ashrrev_i32_e32 v173, 31, v172
	v_lshlrev_b64 v[174:175], 12, v[176:177]
	v_lshl_add_u64 v[178:179], v[172:173], 2, s[36:37]
	v_lshl_add_u64 v[174:175], v[178:179], 0, v[174:175]
	global_load_dwordx4 v[192:195], v[174:175], off nt
	global_load_dwordx4 v[200:203], v[174:175], off offset:16 nt
	global_load_dwordx4 v[204:207], v[174:175], off offset:512 nt
	global_load_dwordx4 v[210:213], v[174:175], off offset:528 nt
	v_or_b32_e32 v196, 16, v176
	v_ashrrev_i32_e32 v197, 31, v196
	v_lshlrev_b64 v[196:197], 12, v[196:197]
	v_lshl_add_u64 v[196:197], v[178:179], 0, v[196:197]
	global_load_dwordx4 v[214:217], v[196:197], off offset:16 nt
	global_load_dwordx4 v[218:221], v[196:197], off nt
	global_load_dwordx4 v[222:225], v[196:197], off offset:528 nt
	global_load_dwordx4 v[226:229], v[196:197], off offset:512 nt
	s_add_i32 s8, s46, 0xffff8800
	s_ashr_i32 s34, s46, 31
	s_cmpk_lt_i32 s33, 0x78
	s_cselect_b32 s35, s34, 0
	s_cselect_b32 s34, s46, s8
	s_cselect_b32 s8, s77, s67
	s_cselect_b32 s33, s76, s66
	s_lshl_b64 s[34:35], s[34:35], 11
	s_add_u32 s34, s33, s34
	s_addc_u32 s35, s8, s35
	v_lshl_add_u64 v[172:173], v[172:173], 1, s[34:35]
	v_lshl_add_u64 v[196:197], v[172:173], 0, v[154:155]
	v_mov_b32_e32 v252, v170
	s_waitcnt vmcnt(0)
	v_pk_mul_f32 v[144:145], v[144:145], v[132:133]
	v_pk_mul_f32 v[142:143], v[142:143], v[130:131]
	v_pk_mul_f32 v[126:127], v[126:127], v[118:119]
	v_pk_mul_f32 v[138:139], v[138:139], v[134:135]
	v_pk_mul_f32 v[230:231], v[122:123], v[114:115]
	v_cvt_pk_bf16_f32 v122, v138, v139
	v_pk_mul_f32 v[140:141], v[140:141], v[136:137]
	v_pk_mul_f32 v[198:199], v[124:125], v[116:117]
	v_cvt_pk_bf16_f32 v123, v140, v141
	v_cvt_pk_bf16_f32 v124, v142, v143
	ds_bpermute_b32 v122, v185, v122
	v_cvt_pk_bf16_f32 v125, v144, v145
	ds_bpermute_b32 v123, v185, v123
	ds_bpermute_b32 v124, v185, v124
	ds_bpermute_b32 v125, v185, v125
	s_waitcnt lgkmcnt(3)
	v_lshlrev_b32_e32 v138, 16, v122
	v_and_b32_e32 v122, 0xffff0000, v122
	s_waitcnt lgkmcnt(2)
	v_lshlrev_b32_e32 v139, 16, v123
	v_and_b32_e32 v123, 0xffff0000, v123
	s_waitcnt lgkmcnt(1)
	v_lshlrev_b32_e32 v140, 16, v124
	v_and_b32_e32 v124, 0xffff0000, v124
	s_waitcnt lgkmcnt(0)
	v_lshlrev_b32_e32 v141, 16, v125
	v_and_b32_e32 v125, 0xffff0000, v125
	v_add_f32_e32 v122, v193, v122
	v_add_f32_e32 v138, v192, v138
	v_add_f32_e32 v123, v195, v123
	v_add_f32_e32 v124, v201, v124
	v_add_f32_e32 v125, v203, v125
	v_cvt_pk_bf16_f32 v122, v138, v122
	v_add_f32_e32 v139, v194, v139
	v_add_f32_e32 v140, v200, v140
	v_add_f32_e32 v141, v202, v141
	v_cvt_pk_bf16_f32 v123, v139, v123
	v_cvt_pk_bf16_f32 v124, v140, v124
	v_cvt_pk_bf16_f32 v125, v141, v125
	global_store_dwordx4 v[196:197], v[122:125], off
	v_pk_mul_f32 v[128:129], v[128:129], v[120:121]
	v_pk_mul_f32 v[110:111], v[110:111], v[134:135]
	v_cvt_pk_bf16_f32 v122, v126, v127
	ds_bpermute_b32 v122, v185, v122
	v_cvt_pk_bf16_f32 v123, v128, v129
	v_cvt_pk_bf16_f32 v124, v230, v231
	ds_bpermute_b32 v123, v185, v123
	ds_bpermute_b32 v124, v185, v124
	v_cvt_pk_bf16_f32 v125, v198, v199
	ds_bpermute_b32 v125, v185, v125
	s_waitcnt lgkmcnt(3)
	v_lshlrev_b32_e32 v126, 16, v122
	v_and_b32_e32 v122, 0xffff0000, v122
	v_add_f32_e32 v126, v204, v126
	v_add_f32_e32 v122, v205, v122
	s_waitcnt lgkmcnt(2)
	v_lshlrev_b32_e32 v127, 16, v123
	v_and_b32_e32 v123, 0xffff0000, v123
	v_cvt_pk_bf16_f32 v122, v126, v122
	s_waitcnt lgkmcnt(1)
	v_lshlrev_b32_e32 v126, 16, v124
	v_and_b32_e32 v124, 0xffff0000, v124
	v_add_f32_e32 v123, v207, v123
	v_add_f32_e32 v126, v210, v126
	v_add_f32_e32 v124, v211, v124
	v_add_f32_e32 v127, v206, v127
	v_cvt_pk_bf16_f32 v123, v127, v123
	v_cvt_pk_bf16_f32 v124, v126, v124
	s_waitcnt lgkmcnt(0)
	v_lshlrev_b32_e32 v126, 16, v125
	v_and_b32_e32 v125, 0xffff0000, v125
	v_add_f32_e32 v125, v213, v125
	v_pk_mul_f32 v[106:107], v[106:107], v[130:131]
	v_add_f32_e32 v126, v212, v126
	v_cvt_pk_bf16_f32 v125, v126, v125
	global_store_dwordx4 v[196:197], v[122:125], off offset:256
	v_pk_mul_f32 v[112:113], v[112:113], v[136:137]
	v_cvt_pk_bf16_f32 v110, v110, v111
	v_pk_mul_f32 v[108:109], v[108:109], v[132:133]
	v_cvt_pk_bf16_f32 v111, v112, v113
	v_cvt_pk_bf16_f32 v106, v106, v107
	ds_bpermute_b32 v107, v185, v110
	v_cvt_pk_bf16_f32 v108, v108, v109
	ds_bpermute_b32 v109, v185, v111
	ds_bpermute_b32 v110, v185, v106
	ds_bpermute_b32 v111, v185, v108
	s_waitcnt lgkmcnt(3)
	v_lshlrev_b32_e32 v106, 16, v107
	v_and_b32_e32 v107, 0xffff0000, v107
	v_add_f32_e32 v106, v218, v106
	v_add_f32_e32 v107, v219, v107
	v_cvt_pk_bf16_f32 v106, v106, v107
	s_waitcnt lgkmcnt(2)
	v_lshlrev_b32_e32 v107, 16, v109
	v_and_b32_e32 v108, 0xffff0000, v109
	v_add_f32_e32 v107, v220, v107
	v_add_f32_e32 v108, v221, v108
	v_cvt_pk_bf16_f32 v107, v107, v108
	s_waitcnt lgkmcnt(1)
	v_lshlrev_b32_e32 v108, 16, v110
	v_and_b32_e32 v109, 0xffff0000, v110
	v_add_f32_e32 v108, v214, v108
	v_add_f32_e32 v109, v215, v109
	v_cvt_pk_bf16_f32 v108, v108, v109
	s_waitcnt lgkmcnt(0)
	v_lshlrev_b32_e32 v109, 16, v111
	v_lshl_add_u64 v[122:123], v[172:173], 0, v[156:157]
	v_add_f32_e32 v109, v216, v109
	v_and_b32_e32 v110, 0xffff0000, v111
	v_pk_mul_f32 v[102:103], v[102:103], v[118:119]
	v_pk_mul_f32 v[98:99], v[98:99], v[114:115]
	v_add_f32_e32 v110, v217, v110
	v_cvt_pk_bf16_f32 v109, v109, v110
	global_store_dwordx4 v[122:123], v[106:109], off
	v_pk_mul_f32 v[104:105], v[104:105], v[120:121]
	v_cvt_pk_bf16_f32 v102, v102, v103
	v_pk_mul_f32 v[100:101], v[100:101], v[116:117]
	v_cvt_pk_bf16_f32 v103, v104, v105
	v_cvt_pk_bf16_f32 v98, v98, v99
	ds_bpermute_b32 v99, v185, v102
	v_cvt_pk_bf16_f32 v100, v100, v101
	ds_bpermute_b32 v101, v185, v103
	ds_bpermute_b32 v102, v185, v98
	ds_bpermute_b32 v103, v185, v100
	s_waitcnt lgkmcnt(3)
	v_lshlrev_b32_e32 v98, 16, v99
	v_and_b32_e32 v99, 0xffff0000, v99
	v_add_f32_e32 v98, v226, v98
	v_add_f32_e32 v99, v227, v99
	v_cvt_pk_bf16_f32 v98, v98, v99
	s_waitcnt lgkmcnt(2)
	v_lshlrev_b32_e32 v99, 16, v101
	v_and_b32_e32 v100, 0xffff0000, v101
	v_add_f32_e32 v99, v228, v99
	v_add_f32_e32 v100, v229, v100
	v_cvt_pk_bf16_f32 v99, v99, v100
	s_waitcnt lgkmcnt(1)
	v_lshlrev_b32_e32 v100, 16, v102
	v_and_b32_e32 v101, 0xffff0000, v102
	v_add_f32_e32 v100, v222, v100
	v_add_f32_e32 v101, v223, v101
	v_cvt_pk_bf16_f32 v100, v100, v101
	s_waitcnt lgkmcnt(0)
	v_lshlrev_b32_e32 v101, 16, v103
	v_add_f32_e32 v101, v224, v101
	v_and_b32_e32 v102, 0xffff0000, v103
	v_add_f32_e32 v102, v225, v102
	v_cvt_pk_bf16_f32 v101, v101, v102
	global_store_dwordx4 v[122:123], v[98:101], off offset:256
	v_or_b32_e32 v122, 48, v176
	v_ashrrev_i32_e32 v123, 31, v122
	v_or_b32_e32 v98, 32, v176
	v_ashrrev_i32_e32 v99, 31, v98
	v_lshlrev_b64 v[98:99], 12, v[98:99]
	v_lshl_add_u64 v[110:111], v[178:179], 0, v[98:99]
	global_load_dwordx4 v[98:101], v[110:111], off nt
	global_load_dwordx4 v[102:105], v[110:111], off offset:16 nt
	global_load_dwordx4 v[106:109], v[110:111], off offset:512 nt
	s_nop 0
	global_load_dwordx4 v[110:113], v[110:111], off offset:528 nt
	v_lshlrev_b64 v[122:123], 12, v[122:123]
	v_lshl_add_u64 v[142:143], v[178:179], 0, v[122:123]
	global_load_dwordx4 v[122:125], v[142:143], off offset:16 nt
	global_load_dwordx4 v[126:129], v[142:143], off nt
	global_load_dwordx4 v[138:141], v[142:143], off offset:528 nt
	s_nop 0
	global_load_dwordx4 v[142:145], v[142:143], off offset:512 nt
	v_pk_mul_f32 v[94:95], v[94:95], v[134:135]
	v_pk_mul_f32 v[90:91], v[90:91], v[130:131]
	v_pk_mul_f32 v[96:97], v[96:97], v[136:137]
	v_cvt_pk_bf16_f32 v94, v94, v95
	v_pk_mul_f32 v[92:93], v[92:93], v[132:133]
	v_cvt_pk_bf16_f32 v95, v96, v97
	v_cvt_pk_bf16_f32 v90, v90, v91
	ds_bpermute_b32 v91, v185, v94
	v_cvt_pk_bf16_f32 v92, v92, v93
	ds_bpermute_b32 v93, v185, v95
	ds_bpermute_b32 v94, v185, v90
	ds_bpermute_b32 v95, v185, v92
	s_waitcnt lgkmcnt(3)
	v_lshlrev_b32_e32 v90, 16, v91
	v_and_b32_e32 v91, 0xffff0000, v91
	s_waitcnt lgkmcnt(2)
	v_and_b32_e32 v92, 0xffff0000, v93
	v_lshl_add_u64 v[176:177], v[172:173], 0, v[158:159]
	v_pk_mul_f32 v[86:87], v[86:87], v[118:119]
	v_pk_mul_f32 v[82:83], v[82:83], v[114:115]
	v_pk_mul_f32 v[88:89], v[88:89], v[120:121]
	v_pk_mul_f32 v[84:85], v[84:85], v[116:117]
	v_pk_mul_f32 v[78:79], v[78:79], v[134:135]
	v_pk_mul_f32 v[74:75], v[74:75], v[130:131]
	v_pk_mul_f32 v[80:81], v[80:81], v[136:137]
	v_pk_mul_f32 v[76:77], v[76:77], v[132:133]
	v_pk_mul_f32 v[70:71], v[70:71], v[118:119]
	v_pk_mul_f32 v[66:67], v[66:67], v[114:115]
	v_pk_mul_f32 v[72:73], v[72:73], v[120:121]
	v_pk_mul_f32 v[68:69], v[68:69], v[116:117]
	v_pk_mul_f32 v[54:55], v[54:55], v[134:135]
	v_pk_mul_f32 v[50:51], v[50:51], v[130:131]
	v_pk_mul_f32 v[56:57], v[56:57], v[136:137]
	v_pk_mul_f32 v[52:53], v[52:53], v[132:133]
	v_pk_mul_f32 v[38:39], v[38:39], v[134:135]
	v_pk_mul_f32 v[34:35], v[34:35], v[130:131]
	v_pk_mul_f32 v[40:41], v[40:41], v[136:137]
	v_pk_mul_f32 v[36:37], v[36:37], v[132:133]
	v_pk_mul_f32 v[22:23], v[22:23], v[134:135]
	v_pk_mul_f32 v[18:19], v[18:19], v[130:131]
	v_pk_mul_f32 v[24:25], v[24:25], v[136:137]
	v_pk_mul_f32 v[20:21], v[20:21], v[132:133]
	v_pk_mul_f32 v[6:7], v[6:7], v[134:135]
	v_pk_mul_f32 v[2:3], v[2:3], v[130:131]
	v_pk_mul_f32 v[8:9], v[8:9], v[136:137]
	v_pk_mul_f32 v[4:5], v[4:5], v[132:133]
	s_waitcnt vmcnt(7)
	v_add_f32_e32 v90, v98, v90
	v_add_f32_e32 v91, v99, v91
	v_cvt_pk_bf16_f32 v90, v90, v91
	v_lshlrev_b32_e32 v91, 16, v93
	v_add_f32_e32 v91, v100, v91
	v_add_f32_e32 v92, v101, v92
	v_cvt_pk_bf16_f32 v91, v91, v92
	s_waitcnt lgkmcnt(1)
	v_lshlrev_b32_e32 v92, 16, v94
	v_and_b32_e32 v93, 0xffff0000, v94
	s_waitcnt vmcnt(6)
	v_add_f32_e32 v92, v102, v92
	v_add_f32_e32 v93, v103, v93
	v_cvt_pk_bf16_f32 v92, v92, v93
	s_waitcnt lgkmcnt(0)
	v_lshlrev_b32_e32 v93, 16, v95
	v_add_f32_e32 v93, v104, v93
	v_and_b32_e32 v94, 0xffff0000, v95
	v_add_f32_e32 v94, v105, v94
	v_cvt_pk_bf16_f32 v93, v93, v94
	global_store_dwordx4 v[176:177], v[90:93], off
	v_cvt_pk_bf16_f32 v86, v86, v87
	v_cvt_pk_bf16_f32 v87, v88, v89
	v_cvt_pk_bf16_f32 v82, v82, v83
	ds_bpermute_b32 v83, v185, v86
	v_cvt_pk_bf16_f32 v84, v84, v85
	ds_bpermute_b32 v85, v185, v87
	ds_bpermute_b32 v86, v185, v82
	ds_bpermute_b32 v87, v185, v84
	s_waitcnt lgkmcnt(3)
	v_lshlrev_b32_e32 v82, 16, v83
	v_and_b32_e32 v83, 0xffff0000, v83
	s_waitcnt vmcnt(6)
	v_add_f32_e32 v82, v106, v82
	v_add_f32_e32 v83, v107, v83
	v_cvt_pk_bf16_f32 v82, v82, v83
	s_waitcnt lgkmcnt(2)
	v_lshlrev_b32_e32 v83, 16, v85
	v_and_b32_e32 v84, 0xffff0000, v85
	v_add_f32_e32 v83, v108, v83
	v_add_f32_e32 v84, v109, v84
	v_cvt_pk_bf16_f32 v83, v83, v84
	s_waitcnt lgkmcnt(1)
	v_lshlrev_b32_e32 v84, 16, v86
	v_and_b32_e32 v85, 0xffff0000, v86
	s_waitcnt vmcnt(5)
	v_add_f32_e32 v84, v110, v84
	v_add_f32_e32 v85, v111, v85
	v_cvt_pk_bf16_f32 v84, v84, v85
	s_waitcnt lgkmcnt(0)
	v_lshlrev_b32_e32 v85, 16, v87
	v_add_f32_e32 v85, v112, v85
	v_and_b32_e32 v86, 0xffff0000, v87
	v_add_f32_e32 v86, v113, v86
	v_cvt_pk_bf16_f32 v85, v85, v86
	global_store_dwordx4 v[176:177], v[82:85], off offset:256
	v_cvt_pk_bf16_f32 v78, v78, v79
	v_cvt_pk_bf16_f32 v79, v80, v81
	v_cvt_pk_bf16_f32 v74, v74, v75
	ds_bpermute_b32 v75, v185, v78
	v_cvt_pk_bf16_f32 v76, v76, v77
	ds_bpermute_b32 v77, v185, v79
	ds_bpermute_b32 v78, v185, v74
	ds_bpermute_b32 v79, v185, v76
	s_waitcnt lgkmcnt(3)
	v_lshlrev_b32_e32 v74, 16, v75
	v_and_b32_e32 v75, 0xffff0000, v75
	s_waitcnt vmcnt(4)
	v_add_f32_e32 v74, v126, v74
	v_add_f32_e32 v75, v127, v75
	v_cvt_pk_bf16_f32 v74, v74, v75
	s_waitcnt lgkmcnt(2)
	v_lshlrev_b32_e32 v75, 16, v77
	v_and_b32_e32 v76, 0xffff0000, v77
	v_add_f32_e32 v75, v128, v75
	v_add_f32_e32 v76, v129, v76
	v_cvt_pk_bf16_f32 v75, v75, v76
	s_waitcnt lgkmcnt(1)
	v_lshlrev_b32_e32 v76, 16, v78
	v_and_b32_e32 v77, 0xffff0000, v78
	v_add_f32_e32 v76, v122, v76
	v_add_f32_e32 v77, v123, v77
	v_cvt_pk_bf16_f32 v76, v76, v77
	s_waitcnt lgkmcnt(0)
	v_lshlrev_b32_e32 v77, 16, v79
	v_lshl_add_u64 v[82:83], v[172:173], 0, v[160:161]
	v_add_f32_e32 v77, v124, v77
	v_and_b32_e32 v78, 0xffff0000, v79
	v_add_f32_e32 v78, v125, v78
	v_cvt_pk_bf16_f32 v77, v77, v78
	global_store_dwordx4 v[82:83], v[74:77], off
	v_cvt_pk_bf16_f32 v70, v70, v71
	v_cvt_pk_bf16_f32 v71, v72, v73
	v_cvt_pk_bf16_f32 v66, v66, v67
	ds_bpermute_b32 v67, v185, v70
	v_cvt_pk_bf16_f32 v68, v68, v69
	ds_bpermute_b32 v69, v185, v71
	ds_bpermute_b32 v70, v185, v66
	ds_bpermute_b32 v71, v185, v68
	s_waitcnt lgkmcnt(3)
	v_lshlrev_b32_e32 v66, 16, v67
	v_and_b32_e32 v67, 0xffff0000, v67
	s_waitcnt vmcnt(3)
	v_add_f32_e32 v66, v142, v66
	v_add_f32_e32 v67, v143, v67
	v_cvt_pk_bf16_f32 v66, v66, v67
	s_waitcnt lgkmcnt(2)
	v_lshlrev_b32_e32 v67, 16, v69
	v_and_b32_e32 v68, 0xffff0000, v69
	v_add_f32_e32 v67, v144, v67
	v_add_f32_e32 v68, v145, v68
	v_cvt_pk_bf16_f32 v67, v67, v68
	s_waitcnt lgkmcnt(1)
	v_lshlrev_b32_e32 v68, 16, v70
	v_and_b32_e32 v69, 0xffff0000, v70
	v_add_f32_e32 v68, v138, v68
	v_add_f32_e32 v69, v139, v69
	v_cvt_pk_bf16_f32 v68, v68, v69
	s_waitcnt lgkmcnt(0)
	v_lshlrev_b32_e32 v69, 16, v71
	v_add_f32_e32 v69, v140, v69
	v_and_b32_e32 v70, 0xffff0000, v71
	v_add_f32_e32 v70, v141, v70
	v_cvt_pk_bf16_f32 v69, v69, v70
	global_store_dwordx4 v[82:83], v[66:69], off offset:256
	v_lshl_add_u64 v[78:79], v[174:175], 0, s[24:25]
	v_lshl_add_u64 v[94:95], v[174:175], 0, s[28:29]
	v_add_co_u32_e32 v66, vcc, s81, v174
	v_lshl_add_u64 v[98:99], v[172:173], 0, v[162:163]
	s_nop 0
	v_addc_co_u32_e32 v67, vcc, 0, v175, vcc
	global_load_dwordx4 v[66:69], v[66:67], off nt
	s_nop 0
	global_load_dwordx4 v[70:73], v[78:79], off offset:16 nt
	global_load_dwordx4 v[74:77], v[78:79], off offset:512 nt
	s_nop 0
	global_load_dwordx4 v[78:81], v[78:79], off offset:528 nt
	v_add_co_u32_e32 v82, vcc, s82, v174
	s_nop 1
	v_addc_co_u32_e32 v83, vcc, 0, v175, vcc
	global_load_dwordx4 v[82:85], v[82:83], off nt
	s_nop 0
	global_load_dwordx4 v[86:89], v[94:95], off offset:528 nt
	global_load_dwordx4 v[90:93], v[94:95], off offset:16 nt
	s_nop 0
	global_load_dwordx4 v[94:97], v[94:95], off offset:512 nt
	v_cvt_pk_bf16_f32 v54, v54, v55
	v_cvt_pk_bf16_f32 v55, v56, v57
	v_cvt_pk_bf16_f32 v50, v50, v51
	ds_bpermute_b32 v51, v185, v54
	v_cvt_pk_bf16_f32 v52, v52, v53
	ds_bpermute_b32 v53, v185, v55
	ds_bpermute_b32 v54, v185, v50
	ds_bpermute_b32 v55, v185, v52
	s_waitcnt lgkmcnt(3)
	v_lshlrev_b32_e32 v50, 16, v51
	v_and_b32_e32 v51, 0xffff0000, v51
	s_waitcnt lgkmcnt(2)
	v_and_b32_e32 v52, 0xffff0000, v53
	v_pk_mul_f32 v[56:57], v[62:63], v[114:115]
	v_lshl_add_u64 v[62:63], v[174:175], 0, s[40:41]
	s_waitcnt vmcnt(7)
	v_add_f32_e32 v50, v66, v50
	v_add_f32_e32 v51, v67, v51
	v_cvt_pk_bf16_f32 v50, v50, v51
	v_lshlrev_b32_e32 v51, 16, v53
	v_add_f32_e32 v51, v68, v51
	v_add_f32_e32 v52, v69, v52
	v_cvt_pk_bf16_f32 v51, v51, v52
	s_waitcnt lgkmcnt(1)
	v_lshlrev_b32_e32 v52, 16, v54
	v_and_b32_e32 v53, 0xffff0000, v54
	s_waitcnt vmcnt(6)
	v_add_f32_e32 v52, v70, v52
	v_add_f32_e32 v53, v71, v53
	v_cvt_pk_bf16_f32 v52, v52, v53
	s_waitcnt lgkmcnt(0)
	v_lshlrev_b32_e32 v53, 16, v55
	v_add_f32_e32 v53, v72, v53
	v_and_b32_e32 v54, 0xffff0000, v55
	v_add_f32_e32 v54, v73, v54
	v_cvt_pk_bf16_f32 v53, v53, v54
	global_store_dwordx4 v[98:99], v[50:53], off
	v_pk_mul_f32 v[54:55], v[64:65], v[116:117]
	v_lshl_add_u64 v[66:67], v[172:173], 0, v[166:167]
	v_pk_mul_f32 v[52:53], v[58:59], v[118:119]
	v_pk_mul_f32 v[50:51], v[60:61], v[120:121]
	v_cvt_pk_bf16_f32 v52, v52, v53
	ds_bpermute_b32 v52, v185, v52
	v_cvt_pk_bf16_f32 v50, v50, v51
	v_cvt_pk_bf16_f32 v51, v56, v57
	v_cvt_pk_bf16_f32 v53, v54, v55
	ds_bpermute_b32 v54, v185, v50
	ds_bpermute_b32 v55, v185, v51
	s_waitcnt lgkmcnt(2)
	v_lshlrev_b32_e32 v50, 16, v52
	v_and_b32_e32 v51, 0xffff0000, v52
	ds_bpermute_b32 v53, v185, v53
	s_waitcnt vmcnt(6)
	v_add_f32_e32 v50, v74, v50
	v_add_f32_e32 v51, v75, v51
	v_cvt_pk_bf16_f32 v50, v50, v51
	s_waitcnt lgkmcnt(2)
	v_lshlrev_b32_e32 v51, 16, v54
	v_and_b32_e32 v52, 0xffff0000, v54
	v_add_f32_e32 v51, v76, v51
	v_add_f32_e32 v52, v77, v52
	v_cvt_pk_bf16_f32 v51, v51, v52
	s_waitcnt lgkmcnt(1)
	v_lshlrev_b32_e32 v52, 16, v55
	v_and_b32_e32 v54, 0xffff0000, v55
	s_waitcnt vmcnt(5)
	v_add_f32_e32 v52, v78, v52
	v_add_f32_e32 v54, v79, v54
	v_cvt_pk_bf16_f32 v52, v52, v54
	s_waitcnt lgkmcnt(0)
	v_lshlrev_b32_e32 v54, 16, v53
	v_and_b32_e32 v53, 0xffff0000, v53
	v_add_f32_e32 v53, v81, v53
	v_add_f32_e32 v54, v80, v54
	v_cvt_pk_bf16_f32 v53, v54, v53
	global_store_dwordx4 v[98:99], v[50:53], off offset:256
	v_cvt_pk_bf16_f32 v38, v38, v39
	v_cvt_pk_bf16_f32 v39, v40, v41
	v_cvt_pk_bf16_f32 v34, v34, v35
	ds_bpermute_b32 v35, v185, v38
	v_cvt_pk_bf16_f32 v36, v36, v37
	ds_bpermute_b32 v37, v185, v39
	ds_bpermute_b32 v38, v185, v34
	ds_bpermute_b32 v39, v185, v36
	s_waitcnt lgkmcnt(3)
	v_lshlrev_b32_e32 v34, 16, v35
	v_and_b32_e32 v35, 0xffff0000, v35
	s_waitcnt vmcnt(5)
	v_add_f32_e32 v34, v82, v34
	v_add_f32_e32 v35, v83, v35
	v_cvt_pk_bf16_f32 v34, v34, v35
	s_waitcnt lgkmcnt(2)
	v_lshlrev_b32_e32 v35, 16, v37
	v_and_b32_e32 v36, 0xffff0000, v37
	v_add_f32_e32 v35, v84, v35
	v_add_f32_e32 v36, v85, v36
	v_cvt_pk_bf16_f32 v35, v35, v36
	s_waitcnt lgkmcnt(1)
	v_lshlrev_b32_e32 v36, 16, v38
	v_and_b32_e32 v37, 0xffff0000, v38
	s_waitcnt vmcnt(3)
	v_add_f32_e32 v36, v90, v36
	v_add_f32_e32 v37, v91, v37
	v_cvt_pk_bf16_f32 v36, v36, v37
	s_waitcnt lgkmcnt(0)
	v_lshlrev_b32_e32 v37, 16, v39
	v_add_f32_e32 v37, v92, v37
	v_and_b32_e32 v38, 0xffff0000, v39
	v_lshl_add_u64 v[50:51], v[172:173], 0, v[164:165]
	v_add_f32_e32 v38, v93, v38
	v_cvt_pk_bf16_f32 v37, v37, v38
	global_store_dwordx4 v[50:51], v[34:37], off
	v_pk_mul_f32 v[38:39], v[48:49], v[116:117]
	v_pk_mul_f32 v[40:41], v[46:47], v[114:115]
	v_pk_mul_f32 v[36:37], v[42:43], v[118:119]
	v_pk_mul_f32 v[34:35], v[44:45], v[120:121]
	v_cvt_pk_bf16_f32 v36, v36, v37
	ds_bpermute_b32 v36, v185, v36
	v_cvt_pk_bf16_f32 v34, v34, v35
	v_cvt_pk_bf16_f32 v35, v40, v41
	v_cvt_pk_bf16_f32 v37, v38, v39
	ds_bpermute_b32 v38, v185, v34
	ds_bpermute_b32 v39, v185, v35
	s_waitcnt lgkmcnt(2)
	v_lshlrev_b32_e32 v34, 16, v36
	v_and_b32_e32 v35, 0xffff0000, v36
	ds_bpermute_b32 v37, v185, v37
	s_waitcnt vmcnt(3)
	v_add_f32_e32 v34, v94, v34
	v_add_f32_e32 v35, v95, v35
	v_cvt_pk_bf16_f32 v34, v34, v35
	s_waitcnt lgkmcnt(2)
	v_lshlrev_b32_e32 v35, 16, v38
	v_and_b32_e32 v36, 0xffff0000, v38
	v_add_f32_e32 v35, v96, v35
	v_add_f32_e32 v36, v97, v36
	v_cvt_pk_bf16_f32 v35, v35, v36
	s_waitcnt lgkmcnt(1)
	v_lshlrev_b32_e32 v36, 16, v39
	v_and_b32_e32 v38, 0xffff0000, v39
	v_add_f32_e32 v36, v86, v36
	v_add_f32_e32 v38, v87, v38
	v_cvt_pk_bf16_f32 v36, v36, v38
	s_waitcnt lgkmcnt(0)
	v_lshlrev_b32_e32 v38, 16, v37
	v_and_b32_e32 v37, 0xffff0000, v37
	v_add_f32_e32 v37, v89, v37
	v_add_f32_e32 v38, v88, v38
	v_cvt_pk_bf16_f32 v37, v38, v37
	global_store_dwordx4 v[50:51], v[34:37], off offset:256
	v_lshl_add_u64 v[46:47], v[174:175], 0, s[38:39]
	s_nop 0
	v_add_co_u32_e32 v34, vcc, s83, v174
	s_nop 1
	v_addc_co_u32_e32 v35, vcc, 0, v175, vcc
	global_load_dwordx4 v[34:37], v[34:35], off nt
	s_nop 0
	global_load_dwordx4 v[38:41], v[46:47], off offset:16 nt
	global_load_dwordx4 v[42:45], v[46:47], off offset:512 nt
	s_nop 0
	global_load_dwordx4 v[46:49], v[46:47], off offset:528 nt
	v_add_co_u32_e32 v50, vcc, s84, v174
	s_nop 1
	v_addc_co_u32_e32 v51, vcc, 0, v175, vcc
	global_load_dwordx4 v[50:53], v[50:51], off nt
	s_nop 0
	global_load_dwordx4 v[54:57], v[62:63], off offset:528 nt
	global_load_dwordx4 v[58:61], v[62:63], off offset:16 nt
	s_nop 0
	global_load_dwordx4 v[62:65], v[62:63], off offset:512 nt
	v_cvt_pk_bf16_f32 v22, v22, v23
	v_cvt_pk_bf16_f32 v23, v24, v25
	v_cvt_pk_bf16_f32 v18, v18, v19
	ds_bpermute_b32 v19, v185, v22
	v_cvt_pk_bf16_f32 v20, v20, v21
	ds_bpermute_b32 v21, v185, v23
	ds_bpermute_b32 v22, v185, v18
	ds_bpermute_b32 v23, v185, v20
	s_waitcnt lgkmcnt(3)
	v_lshlrev_b32_e32 v18, 16, v19
	v_and_b32_e32 v19, 0xffff0000, v19
	s_waitcnt lgkmcnt(2)
	v_and_b32_e32 v20, 0xffff0000, v21
	v_pk_mul_f32 v[24:25], v[30:31], v[114:115]
	s_and_b64 vcc, exec, s[0:1]
	s_mov_b64 s[0:1], -1
	s_waitcnt vmcnt(7)
; #define PG8_BAR __builtin_amdgcn_s_barrier()
; template <class Epi, class Sched, bool GATHER, bool DUAL = false>
; __device__ __forceinline__ void gemm_phase(LAS unsigned char* lds, const Gemm g, const Sched& S, const Epi& E) {
;     ...
;         cur = nxt; cB = nB; cAb = nAb; ++ui; nxt = n2; has_next = has_n2;
; #pragma unroll
;         for (int h = 0; h < 2; ++h)
; #pragma unroll
;             for (int i = 0; i < 2; ++i) cofs[h][i] = nofs[h][i];
;         if (wr == 1) PG8_BAR;
	v_add_f32_e32 v18, v34, v18
	v_add_f32_e32 v19, v35, v19
	v_cvt_pk_bf16_f32 v18, v18, v19
	v_lshlrev_b32_e32 v19, 16, v21
	v_add_f32_e32 v19, v36, v19
	v_add_f32_e32 v20, v37, v20
	v_cvt_pk_bf16_f32 v19, v19, v20
	s_waitcnt lgkmcnt(1)
	v_lshlrev_b32_e32 v20, 16, v22
	v_and_b32_e32 v21, 0xffff0000, v22
	s_waitcnt vmcnt(6)
	v_add_f32_e32 v20, v38, v20
	v_add_f32_e32 v21, v39, v21
	v_cvt_pk_bf16_f32 v20, v20, v21
	s_waitcnt lgkmcnt(0)
	v_lshlrev_b32_e32 v21, 16, v23
	v_add_f32_e32 v21, v40, v21
	v_and_b32_e32 v22, 0xffff0000, v23
	v_add_f32_e32 v22, v41, v22
	v_cvt_pk_bf16_f32 v21, v21, v22
	global_store_dwordx4 v[66:67], v[18:21], off
	v_pk_mul_f32 v[22:23], v[32:33], v[116:117]
	s_nop 0
	v_pk_mul_f32 v[20:21], v[26:27], v[118:119]
	v_pk_mul_f32 v[18:19], v[28:29], v[120:121]
	v_cvt_pk_bf16_f32 v20, v20, v21
	ds_bpermute_b32 v20, v185, v20
	v_cvt_pk_bf16_f32 v18, v18, v19
	v_cvt_pk_bf16_f32 v19, v24, v25
	v_cvt_pk_bf16_f32 v21, v22, v23
	ds_bpermute_b32 v22, v185, v18
	ds_bpermute_b32 v23, v185, v19
	s_waitcnt lgkmcnt(2)
	v_lshlrev_b32_e32 v18, 16, v20
	v_and_b32_e32 v19, 0xffff0000, v20
	ds_bpermute_b32 v21, v185, v21
	s_waitcnt vmcnt(6)
	v_add_f32_e32 v18, v42, v18
	v_add_f32_e32 v19, v43, v19
	v_cvt_pk_bf16_f32 v18, v18, v19
	s_waitcnt lgkmcnt(2)
	v_lshlrev_b32_e32 v19, 16, v22
	v_and_b32_e32 v20, 0xffff0000, v22
	v_add_f32_e32 v19, v44, v19
	v_add_f32_e32 v20, v45, v20
	v_cvt_pk_bf16_f32 v19, v19, v20
	s_waitcnt lgkmcnt(1)
	v_lshlrev_b32_e32 v20, 16, v23
	v_and_b32_e32 v22, 0xffff0000, v23
	s_waitcnt vmcnt(5)
	v_add_f32_e32 v20, v46, v20
	v_add_f32_e32 v22, v47, v22
	v_cvt_pk_bf16_f32 v20, v20, v22
	s_waitcnt lgkmcnt(0)
	v_lshlrev_b32_e32 v22, 16, v21
	v_and_b32_e32 v21, 0xffff0000, v21
	v_add_f32_e32 v21, v49, v21
	v_add_f32_e32 v22, v48, v22
	v_cvt_pk_bf16_f32 v21, v22, v21
	global_store_dwordx4 v[66:67], v[18:21], off offset:256
	v_cvt_pk_bf16_f32 v6, v6, v7
	v_cvt_pk_bf16_f32 v7, v8, v9
	v_cvt_pk_bf16_f32 v2, v2, v3
	ds_bpermute_b32 v3, v185, v6
	v_cvt_pk_bf16_f32 v4, v4, v5
	ds_bpermute_b32 v5, v185, v7
	ds_bpermute_b32 v6, v185, v2
	ds_bpermute_b32 v7, v185, v4
	s_waitcnt lgkmcnt(3)
	v_lshlrev_b32_e32 v2, 16, v3
	v_and_b32_e32 v3, 0xffff0000, v3
	s_waitcnt vmcnt(5)
	v_add_f32_e32 v2, v50, v2
	v_add_f32_e32 v3, v51, v3
	v_cvt_pk_bf16_f32 v2, v2, v3
	s_waitcnt lgkmcnt(2)
	v_lshlrev_b32_e32 v3, 16, v5
	v_and_b32_e32 v4, 0xffff0000, v5
	v_add_f32_e32 v3, v52, v3
	v_add_f32_e32 v4, v53, v4
	v_cvt_pk_bf16_f32 v3, v3, v4
	s_waitcnt lgkmcnt(1)
	v_lshlrev_b32_e32 v4, 16, v6
	v_and_b32_e32 v5, 0xffff0000, v6
	s_waitcnt vmcnt(3)
	v_add_f32_e32 v4, v58, v4
	v_add_f32_e32 v5, v59, v5
	v_cvt_pk_bf16_f32 v4, v4, v5
	s_waitcnt lgkmcnt(0)
	v_lshlrev_b32_e32 v5, 16, v7
	v_add_f32_e32 v5, v60, v5
	v_and_b32_e32 v6, 0xffff0000, v7
	v_lshl_add_u64 v[18:19], v[172:173], 0, v[168:169]
	v_add_f32_e32 v6, v61, v6
	v_cvt_pk_bf16_f32 v5, v5, v6
	global_store_dwordx4 v[18:19], v[2:5], off
	v_pk_mul_f32 v[6:7], v[16:17], v[116:117]
	v_pk_mul_f32 v[8:9], v[14:15], v[114:115]
	v_pk_mul_f32 v[4:5], v[10:11], v[118:119]
	v_pk_mul_f32 v[2:3], v[12:13], v[120:121]
	v_cvt_pk_bf16_f32 v4, v4, v5
	ds_bpermute_b32 v4, v185, v4
	v_cvt_pk_bf16_f32 v2, v2, v3
	v_cvt_pk_bf16_f32 v3, v8, v9
	v_cvt_pk_bf16_f32 v5, v6, v7
	ds_bpermute_b32 v6, v185, v2
	ds_bpermute_b32 v7, v185, v3
	s_waitcnt lgkmcnt(2)
	v_lshlrev_b32_e32 v2, 16, v4
	v_and_b32_e32 v3, 0xffff0000, v4
	ds_bpermute_b32 v5, v185, v5
	s_waitcnt vmcnt(3)
	v_add_f32_e32 v2, v62, v2
	v_add_f32_e32 v3, v63, v3
	v_cvt_pk_bf16_f32 v2, v2, v3
	s_waitcnt lgkmcnt(2)
	v_lshlrev_b32_e32 v3, 16, v6
	v_and_b32_e32 v4, 0xffff0000, v6
	v_add_f32_e32 v3, v64, v3
	v_add_f32_e32 v4, v65, v4
	v_cvt_pk_bf16_f32 v3, v3, v4
	s_waitcnt lgkmcnt(1)
	v_lshlrev_b32_e32 v4, 16, v7
	v_and_b32_e32 v6, 0xffff0000, v7
	v_add_f32_e32 v4, v54, v4
	v_add_f32_e32 v6, v55, v6
	v_cvt_pk_bf16_f32 v4, v4, v6
	s_waitcnt lgkmcnt(0)
	v_lshlrev_b32_e32 v6, 16, v5
	v_and_b32_e32 v5, 0xffff0000, v5
	v_add_f32_e32 v5, v57, v5
	v_add_f32_e32 v6, v56, v6
	v_cvt_pk_bf16_f32 v5, v6, v5
	global_store_dwordx4 v[18:19], v[2:5], off offset:256
	s_cbranch_vccnz .LBB0_737
	s_andn2_b64 vcc, exec, s[10:11]
	s_cbranch_vccnz .LBB0_736
	s_barrier
	s_branch .LBB0_736
